# speedup vs baseline: 1.0033x; 1.0033x over previous
.LBB1_4:
	s_mov_b32 s39, s28
	s_mov_b32 s37, s36
	s_mov_b32 s36, s5
	s_cbranch_execz .LBB1_24
	s_branch .LBB1_32
	.p2align	6

.LBB3_12:
	v_add_u32_e32 v160, s6, v69
	v_add_u32_e32 v161, s10, v69
	v_add_u32_e32 v162, v160, v67
	v_add_u32_e32 v163, v161, v67
	v_add_u32_e32 v164, v160, v68
	v_add_u32_e32 v165, v161, v68
	s_lshl_b32 s12, s11, 15
	v_add_u32_e32 v166, s12, v162
	v_add_u32_e32 v167, s12, v163
	ds_read_b128 v[96:99], v167 offset:16384
	ds_read_b128 v[100:103], v167 offset:18432
	ds_read_b128 v[104:107], v167 offset:20480
	ds_read_b128 v[108:111], v167 offset:22528
	ds_read_b128 v[112:115], v166
	ds_read_b128 v[116:119], v166 offset:2048
	ds_read_b128 v[120:123], v166 offset:4096
	ds_read_b128 v[124:127], v166 offset:6144
	.p2align	6
